# back-edge rotation (docs 7.11): K-loop counter/pointer updates and exit test moved in front of the loop-back barrier in the P1, P3, P6, P8, P9 GEMM loops
# speedup vs baseline: 1.0043x; 1.0043x over previous
; #define PG8_STAGE(bufoff, gbase, voff) do { _Pragma("unroll") for (int _i = 0; _i < 2; ++_i) \
;         __builtin_amdgcn_global_load_lds((const unsigned*)((const char*)(gbase) + (voff)[_i]), (LAS unsigned*)(lds + (bufoff) + ldsw + _i * 8192), 16, 0, 0); } while (0)
; #define PG8_LDA(dst, b, h) do { _Pragma("unroll") for (int m = 0; m < 4; ++m) _Pragma("unroll") for (int k = 0; k < 2; ++k) frag_set(dst[m], k, *(const LAS bf16x8*)(lds + PG8_SA(b, h) + aoff + m * 2048 + k * 1024)); } while (0)
; template <class Epi, class Sched, bool ALIGN_EPI, bool FP8 = false>
; __device__ __forceinline__ void gemm_phase(LAS unsigned char* lds, const Gemm g, const Sched& S, const Epi& E) {
;     ...
;         for (int t = 0; t < nt; t += 2) {
;             const bool last = (t == nt - 2);
;             const char* a1 = Ab + (size_t)(t + 1) * kstep;
;             PG8_LDB(B0, 0, 0); PG8_LDB(B1, 0, 1); PG8_SCHED; PG8_LDA(At, 0, 0); PG8_STAGE(PG8_SA(1, 1), a1, ao[1]);
;             PG8_WAIT_V(8); PG8_WAIT_L(0); PG8_BAR; if (do0) { PG8_MMA(0, 0, At, B0); PG8_MMA(0, 1, At, B1); } PG8_BAR; PG8_SCHED;
;             const char* a2 = last ? Ab : Ab + (size_t)(t + 2) * kstep; const char* b2 = last ? nB : cB + (size_t)(t + 2) * kstep;
;             if (last && has_next) { int t2 = tid; asm volatile("" : "+v"(t2)); int R2[2], C2[2];
; #pragma unroll
;                 for (int i = 0; i < 2; ++i) stage_rc(t2 * 16 + i * 8192, R2[i], C2[i]);
;                 S.a_off_next(nxt, R2, C2, ao, lds + AUX_OFF); }
;             const char* a3 = a2 + kstep; const char* b3 = b2 + kstep;
;             PG8_LDA(At, 0, 1); PG8_STAGE(PG8_SB(0, 0), b2, voffB); PG8_STAGE(PG8_SB(0, 1), b2 + hstep, voffB); PG8_STAGE(PG8_SA(0, 0), a2, ao[0]);
;             PG8_WAIT_V(8); PG8_WAIT_L(0); PG8_BAR; if (full) { PG8_MMA(1, 0, At, B0); PG8_MMA(1, 1, At, B1); } PG8_BAR; PG8_SCHED;
;             PG8_LDB(B0, 1, 0); PG8_LDB(B1, 1, 1); PG8_SCHED; PG8_LDA(At, 1, 0); PG8_STAGE(PG8_SA(0, 1), a2, ao[1]);
;             PG8_WAIT_V(8); PG8_WAIT_L(0); PG8_BAR; if (do0) { PG8_MMA(0, 0, At, B0); PG8_MMA(0, 1, At, B1); } PG8_BAR; PG8_SCHED;
;             PG8_LDA(At, 1, 1); PG8_STAGE(PG8_SB(1, 0), b3, voffB); PG8_STAGE(PG8_SB(1, 1), b3 + hstep, voffB); PG8_STAGE(PG8_SA(1, 0), a3, ao[0]);
;             PG8_WAIT_V(8); PG8_WAIT_L(0); PG8_BAR; if (full) { PG8_MMA(1, 0, At, B0); PG8_MMA(1, 1, At, B1); } PG8_BAR; PG8_SCHED;
.LBB0_180:
	s_add_i32 s90, s90, 2
	s_add_u32 s88, s88, 0x100
	s_addc_u32 s89, s89, 0
	s_add_u32 s64, s64, 0x100
	s_addc_u32 s65, s65, 0
	s_cmp_gt_u32 s90, 29
	s_barrier
	s_cbranch_scc1 .LBB0_191

; #define PG8_STAGE(bufoff, gbase, voff) do { _Pragma("unroll") for (int _i = 0; _i < 2; ++_i) \
;         __builtin_amdgcn_global_load_lds((const unsigned*)((const char*)(gbase) + (voff)[_i]), (LAS unsigned*)(lds + (bufoff) + ldsw + _i * 8192), 16, 0, 0); } while (0)
; template <class Epi, class Sched, bool ALIGN_EPI, bool FP8 = false>
; __device__ __forceinline__ void gemm_phase(LAS unsigned char* lds, const Gemm g, const Sched& S, const Epi& E) {
;     ...
;         for (int t = 0; t < nt; t += 2) {
;             const bool last = (t == nt - 2);
;             const char* a1 = Ab + (size_t)(t + 1) * kstep;
;             PG8_LDB(B0, 0, 0); PG8_LDB(B1, 0, 1); PG8_SCHED; PG8_LDA(At, 0, 0); PG8_STAGE(PG8_SA(1, 1), a1, ao[1]);
;             PG8_WAIT_V(8); PG8_WAIT_L(0); PG8_BAR; if (do0) { PG8_MMA(0, 0, At, B0); PG8_MMA(0, 1, At, B1); } PG8_BAR; PG8_SCHED;
;             const char* a2 = last ? Ab : Ab + (size_t)(t + 2) * kstep; const char* b2 = last ? nB : cB + (size_t)(t + 2) * kstep;
;             if (last && has_next) { int t2 = tid; asm volatile("" : "+v"(t2)); int R2[2], C2[2];
; #pragma unroll
;                 for (int i = 0; i < 2; ++i) stage_rc(t2 * 16 + i * 8192, R2[i], C2[i]);
;                 S.a_off_next(nxt, R2, C2, ao, lds + AUX_OFF); }
;             const char* a3 = a2 + kstep; const char* b3 = b2 + kstep;
;             PG8_LDA(At, 0, 1); PG8_STAGE(PG8_SB(0, 0), b2, voffB); PG8_STAGE(PG8_SB(0, 1), b2 + hstep, voffB); PG8_STAGE(PG8_SA(0, 0), a2, ao[0]);
;             PG8_WAIT_V(8); PG8_WAIT_L(0); PG8_BAR; if (full) { PG8_MMA(1, 0, At, B0); PG8_MMA(1, 1, At, B1); } PG8_BAR; PG8_SCHED;
;             PG8_LDB(B0, 1, 0); PG8_LDB(B1, 1, 1); PG8_SCHED; PG8_LDA(At, 1, 0); PG8_STAGE(PG8_SA(0, 1), a2, ao[1]);
;             PG8_WAIT_V(8); PG8_WAIT_L(0); PG8_BAR; if (do0) { PG8_MMA(0, 0, At, B0); PG8_MMA(0, 1, At, B1); } PG8_BAR; PG8_SCHED;
;             PG8_LDA(At, 1, 1); PG8_STAGE(PG8_SB(1, 0), b3, voffB); PG8_STAGE(PG8_SB(1, 1), b3 + hstep, voffB); PG8_STAGE(PG8_SA(1, 0), a3, ao[0]);
;             PG8_WAIT_V(8); PG8_WAIT_L(0); PG8_BAR; if (full) { PG8_MMA(1, 0, At, B0); PG8_MMA(1, 1, At, B1); } PG8_BAR; PG8_SCHED;
; __device__ __forceinline__ void phase1() { const Ctx c = make_ctx(); PHASE_PTRS;
;     ...
;             const Ctx c3 = make_ctx(); if (c3.tid == 0) __hip_atomic_fetch_add(ctl + CW_PDONE, 1u, __ATOMIC_RELAXED, __HIP_MEMORY_SCOPE_AGENT);
.LBB0_313:
	s_add_i32 s87, s87, 2
	s_add_u32 s85, s85, 0x100
	s_addc_u32 s86, s86, 0
	s_add_u32 s62, s62, 0x100
	s_addc_u32 s63, s63, 0
	s_cmp_eq_u32 s87, 26
	s_cbranch_scc0 .Lp1sig_skip
	s_and_b64 s[98:99], s[4:5], exec
	s_cbranch_scc1 .Lp1sig_skip
	v_readfirstlane_b32 s98, v0
	s_cmp_lg_u32 s98, 0
	s_cbranch_scc1 .Lp1sig_skip
	s_mov_b64 s[98:99], exec
	s_mov_b64 exec, 1
	v_mov_b32_e32 v253, 0x1000
	v_mov_b32_e32 v254, 1
	global_atomic_add v253, v254, s[30:31] offset:1280
	s_mov_b64 exec, s[98:99]
.Lp1sig_skip:
	s_cmp_gt_u32 s87, 29
	s_barrier
	s_cbranch_scc1 .LBB0_324

; #define PG8_STAGE(bufoff, gbase, voff) do { _Pragma("unroll") for (int _i = 0; _i < 2; ++_i) \
;         __builtin_amdgcn_global_load_lds((const unsigned*)((const char*)(gbase) + (voff)[_i]), (LAS unsigned*)(lds + (bufoff) + ldsw + _i * 8192), 16, 0, 0); } while (0)
; #define PG8_LDA(dst, b, h) do { _Pragma("unroll") for (int m = 0; m < 4; ++m) _Pragma("unroll") for (int k = 0; k < 2; ++k) frag_set(dst[m], k, *(const LAS bf16x8*)(lds + PG8_SA(b, h) + aoff + m * 2048 + k * 1024)); } while (0)
; template <class Epi, class Sched, bool ALIGN_EPI, bool FP8 = false>
; __device__ __forceinline__ void gemm_phase(LAS unsigned char* lds, const Gemm g, const Sched& S, const Epi& E) {
;     ...
;         for (int t = 0; t < nt; t += 2) {
;             const bool last = (t == nt - 2);
;             const char* a1 = Ab + (size_t)(t + 1) * kstep;
;             PG8_LDB(B0, 0, 0); PG8_LDB(B1, 0, 1); PG8_SCHED; PG8_LDA(At, 0, 0); PG8_STAGE(PG8_SA(1, 1), a1, ao[1]);
;             PG8_WAIT_V(8); PG8_WAIT_L(0); PG8_BAR; if (do0) { PG8_MMA(0, 0, At, B0); PG8_MMA(0, 1, At, B1); } PG8_BAR; PG8_SCHED;
;             const char* a2 = last ? Ab : Ab + (size_t)(t + 2) * kstep; const char* b2 = last ? nB : cB + (size_t)(t + 2) * kstep;
;             if (last && has_next) { int t2 = tid; asm volatile("" : "+v"(t2)); int R2[2], C2[2];
; #pragma unroll
;                 for (int i = 0; i < 2; ++i) stage_rc(t2 * 16 + i * 8192, R2[i], C2[i]);
;                 S.a_off_next(nxt, R2, C2, ao, lds + AUX_OFF); }
;             const char* a3 = a2 + kstep; const char* b3 = b2 + kstep;
;             PG8_LDA(At, 0, 1); PG8_STAGE(PG8_SB(0, 0), b2, voffB); PG8_STAGE(PG8_SB(0, 1), b2 + hstep, voffB); PG8_STAGE(PG8_SA(0, 0), a2, ao[0]);
;             PG8_WAIT_V(8); PG8_WAIT_L(0); PG8_BAR; if (full) { PG8_MMA(1, 0, At, B0); PG8_MMA(1, 1, At, B1); } PG8_BAR; PG8_SCHED;
;             PG8_LDB(B0, 1, 0); PG8_LDB(B1, 1, 1); PG8_SCHED; PG8_LDA(At, 1, 0); PG8_STAGE(PG8_SA(0, 1), a2, ao[1]);
;             PG8_WAIT_V(8); PG8_WAIT_L(0); PG8_BAR; if (do0) { PG8_MMA(0, 0, At, B0); PG8_MMA(0, 1, At, B1); } PG8_BAR; PG8_SCHED;
;             PG8_LDA(At, 1, 1); PG8_STAGE(PG8_SB(1, 0), b3, voffB); PG8_STAGE(PG8_SB(1, 1), b3 + hstep, voffB); PG8_STAGE(PG8_SA(1, 0), a3, ao[0]);
;             PG8_WAIT_V(8); PG8_WAIT_L(0); PG8_BAR; if (full) { PG8_MMA(1, 0, At, B0); PG8_MMA(1, 1, At, B1); } PG8_BAR; PG8_SCHED;
.LBB0_467:
	s_add_i32 s89, s89, 2
	s_add_u32 s28, s28, 0x100
	s_addc_u32 s29, s29, 0
	s_add_u32 s76, s76, 0x100
	s_addc_u32 s77, s77, 0
	s_cmp_gt_u32 s89, 5
	s_barrier
	s_cbranch_scc1 .LBB0_478

; #define PG8_STAGE(bufoff, gbase, voff) do { _Pragma("unroll") for (int _i = 0; _i < 2; ++_i) \
;         __builtin_amdgcn_global_load_lds((const unsigned*)((const char*)(gbase) + (voff)[_i]), (LAS unsigned*)(lds + (bufoff) + ldsw + _i * 8192), 16, 0, 0); } while (0)
; #define PG8_LDA(dst, b, h) do { _Pragma("unroll") for (int m = 0; m < 4; ++m) _Pragma("unroll") for (int k = 0; k < 2; ++k) frag_set(dst[m], k, *(const LAS bf16x8*)(lds + PG8_SA(b, h) + aoff + m * 2048 + k * 1024)); } while (0)
; template <class Epi, class Sched, bool ALIGN_EPI, bool FP8 = false>
; __device__ __forceinline__ void gemm_phase(LAS unsigned char* lds, const Gemm g, const Sched& S, const Epi& E) {
;     ...
;         for (int t = 0; t < nt; t += 2) {
;             const bool last = (t == nt - 2);
;             const char* a1 = Ab + (size_t)(t + 1) * kstep;
;             PG8_LDB(B0, 0, 0); PG8_LDB(B1, 0, 1); PG8_SCHED; PG8_LDA(At, 0, 0); PG8_STAGE(PG8_SA(1, 1), a1, ao[1]);
;             PG8_WAIT_V(8); PG8_WAIT_L(0); PG8_BAR; if (do0) { PG8_MMA(0, 0, At, B0); PG8_MMA(0, 1, At, B1); } PG8_BAR; PG8_SCHED;
;             const char* a2 = last ? Ab : Ab + (size_t)(t + 2) * kstep; const char* b2 = last ? nB : cB + (size_t)(t + 2) * kstep;
;             if (last && has_next) { int t2 = tid; asm volatile("" : "+v"(t2)); int R2[2], C2[2];
; #pragma unroll
;                 for (int i = 0; i < 2; ++i) stage_rc(t2 * 16 + i * 8192, R2[i], C2[i]);
;                 S.a_off_next(nxt, R2, C2, ao, lds + AUX_OFF); }
;             const char* a3 = a2 + kstep; const char* b3 = b2 + kstep;
;             PG8_LDA(At, 0, 1); PG8_STAGE(PG8_SB(0, 0), b2, voffB); PG8_STAGE(PG8_SB(0, 1), b2 + hstep, voffB); PG8_STAGE(PG8_SA(0, 0), a2, ao[0]);
;             PG8_WAIT_V(8); PG8_WAIT_L(0); PG8_BAR; if (full) { PG8_MMA(1, 0, At, B0); PG8_MMA(1, 1, At, B1); } PG8_BAR; PG8_SCHED;
;             PG8_LDB(B0, 1, 0); PG8_LDB(B1, 1, 1); PG8_SCHED; PG8_LDA(At, 1, 0); PG8_STAGE(PG8_SA(0, 1), a2, ao[1]);
;             PG8_WAIT_V(8); PG8_WAIT_L(0); PG8_BAR; if (do0) { PG8_MMA(0, 0, At, B0); PG8_MMA(0, 1, At, B1); } PG8_BAR; PG8_SCHED;
;             PG8_LDA(At, 1, 1); PG8_STAGE(PG8_SB(1, 0), b3, voffB); PG8_STAGE(PG8_SB(1, 1), b3 + hstep, voffB); PG8_STAGE(PG8_SA(1, 0), a3, ao[0]);
;             PG8_WAIT_V(8); PG8_WAIT_L(0); PG8_BAR; if (full) { PG8_MMA(1, 0, At, B0); PG8_MMA(1, 1, At, B1); } PG8_BAR; PG8_SCHED;
.LBB0_706:
	s_add_i32 s91, s91, 2
	s_add_u32 s28, s28, 0x100
	s_addc_u32 s29, s29, 0
	s_add_u32 s70, s70, 0x100
	s_addc_u32 s71, s71, 0
	s_cmp_gt_u32 s91, 5
	s_barrier
	s_cbranch_scc1 .LBB0_717

; #define PG8_STAGE(bufoff, gbase, voff) do { _Pragma("unroll") for (int _i = 0; _i < 2; ++_i) \
;         __builtin_amdgcn_global_load_lds((const unsigned*)((const char*)(gbase) + (voff)[_i]), (LAS unsigned*)(lds + (bufoff) + ldsw + _i * 8192), 16, 0, 0); } while (0)
; #define PG8_LDA(dst, b, h) do { _Pragma("unroll") for (int m = 0; m < 4; ++m) _Pragma("unroll") for (int k = 0; k < 2; ++k) frag_set(dst[m], k, *(const LAS bf16x8*)(lds + PG8_SA(b, h) + aoff + m * 2048 + k * 1024)); } while (0)
; template <class Epi, class Sched, bool ALIGN_EPI, bool FP8 = false>
; __device__ __forceinline__ void gemm_phase(LAS unsigned char* lds, const Gemm g, const Sched& S, const Epi& E) {
;     ...
;         for (int t = 0; t < nt; t += 2) {
;             const bool last = (t == nt - 2);
;             const char* a1 = Ab + (size_t)(t + 1) * kstep;
;             PG8_LDB(B0, 0, 0); PG8_LDB(B1, 0, 1); PG8_SCHED; PG8_LDA(At, 0, 0); PG8_STAGE(PG8_SA(1, 1), a1, ao[1]);
;             PG8_WAIT_V(8); PG8_WAIT_L(0); PG8_BAR; if (do0) { PG8_MMA(0, 0, At, B0); PG8_MMA(0, 1, At, B1); } PG8_BAR; PG8_SCHED;
;             const char* a2 = last ? Ab : Ab + (size_t)(t + 2) * kstep; const char* b2 = last ? nB : cB + (size_t)(t + 2) * kstep;
;             if (last && has_next) { int t2 = tid; asm volatile("" : "+v"(t2)); int R2[2], C2[2];
; #pragma unroll
;                 for (int i = 0; i < 2; ++i) stage_rc(t2 * 16 + i * 8192, R2[i], C2[i]);
;                 S.a_off_next(nxt, R2, C2, ao, lds + AUX_OFF); }
;             const char* a3 = a2 + kstep; const char* b3 = b2 + kstep;
;             PG8_LDA(At, 0, 1); PG8_STAGE(PG8_SB(0, 0), b2, voffB); PG8_STAGE(PG8_SB(0, 1), b2 + hstep, voffB); PG8_STAGE(PG8_SA(0, 0), a2, ao[0]);
;             PG8_WAIT_V(8); PG8_WAIT_L(0); PG8_BAR; if (full) { PG8_MMA(1, 0, At, B0); PG8_MMA(1, 1, At, B1); } PG8_BAR; PG8_SCHED;
;             PG8_LDB(B0, 1, 0); PG8_LDB(B1, 1, 1); PG8_SCHED; PG8_LDA(At, 1, 0); PG8_STAGE(PG8_SA(0, 1), a2, ao[1]);
;             PG8_WAIT_V(8); PG8_WAIT_L(0); PG8_BAR; if (do0) { PG8_MMA(0, 0, At, B0); PG8_MMA(0, 1, At, B1); } PG8_BAR; PG8_SCHED;
;             PG8_LDA(At, 1, 1); PG8_STAGE(PG8_SB(1, 0), b3, voffB); PG8_STAGE(PG8_SB(1, 1), b3 + hstep, voffB); PG8_STAGE(PG8_SA(1, 0), a3, ao[0]);
;             PG8_WAIT_V(8); PG8_WAIT_L(0); PG8_BAR; if (full) { PG8_MMA(1, 0, At, B0); PG8_MMA(1, 1, At, B1); } PG8_BAR; PG8_SCHED;
.LBB0_1098:
	s_add_i32 s81, s81, 2
	s_add_u32 s79, s79, 0x100
	s_addc_u32 s80, s80, 0
	s_add_u32 s56, s56, 0x100
	s_addc_u32 s57, s57, 0
	s_cmp_gt_u32 s81, 29
	s_barrier
	s_cbranch_scc1 .LBB0_1109

; #define PG8_STAGE(bufoff, gbase, voff) do { _Pragma("unroll") for (int _i = 0; _i < 2; ++_i) \
;         __builtin_amdgcn_global_load_lds((const unsigned*)((const char*)(gbase) + (voff)[_i]), (LAS unsigned*)(lds + (bufoff) + ldsw + _i * 8192), 16, 0, 0); } while (0)
; #define PG8_LDA(dst, b, h) do { _Pragma("unroll") for (int m = 0; m < 4; ++m) _Pragma("unroll") for (int k = 0; k < 2; ++k) frag_set(dst[m], k, *(const LAS bf16x8*)(lds + PG8_SA(b, h) + aoff + m * 2048 + k * 1024)); } while (0)
; template <class Epi, class Sched, bool ALIGN_EPI, bool FP8 = false>
; __device__ __forceinline__ void gemm_phase(LAS unsigned char* lds, const Gemm g, const Sched& S, const Epi& E) {
;     ...
;         for (int t = 0; t < nt; t += 2) {
;             const bool last = (t == nt - 2);
;             const char* a1 = Ab + (size_t)(t + 1) * kstep;
;             PG8_LDB(B0, 0, 0); PG8_LDB(B1, 0, 1); PG8_SCHED; PG8_LDA(At, 0, 0); PG8_STAGE(PG8_SA(1, 1), a1, ao[1]);
;             PG8_WAIT_V(8); PG8_WAIT_L(0); PG8_BAR; if (do0) { PG8_MMA(0, 0, At, B0); PG8_MMA(0, 1, At, B1); } PG8_BAR; PG8_SCHED;
;             const char* a2 = last ? Ab : Ab + (size_t)(t + 2) * kstep; const char* b2 = last ? nB : cB + (size_t)(t + 2) * kstep;
;             if (last && has_next) { int t2 = tid; asm volatile("" : "+v"(t2)); int R2[2], C2[2];
; #pragma unroll
;                 for (int i = 0; i < 2; ++i) stage_rc(t2 * 16 + i * 8192, R2[i], C2[i]);
;                 S.a_off_next(nxt, R2, C2, ao, lds + AUX_OFF); }
;             const char* a3 = a2 + kstep; const char* b3 = b2 + kstep;
;             PG8_LDA(At, 0, 1); PG8_STAGE(PG8_SB(0, 0), b2, voffB); PG8_STAGE(PG8_SB(0, 1), b2 + hstep, voffB); PG8_STAGE(PG8_SA(0, 0), a2, ao[0]);
;             PG8_WAIT_V(8); PG8_WAIT_L(0); PG8_BAR; if (full) { PG8_MMA(1, 0, At, B0); PG8_MMA(1, 1, At, B1); } PG8_BAR; PG8_SCHED;
;             PG8_LDB(B0, 1, 0); PG8_LDB(B1, 1, 1); PG8_SCHED; PG8_LDA(At, 1, 0); PG8_STAGE(PG8_SA(0, 1), a2, ao[1]);
;             PG8_WAIT_V(8); PG8_WAIT_L(0); PG8_BAR; if (do0) { PG8_MMA(0, 0, At, B0); PG8_MMA(0, 1, At, B1); } PG8_BAR; PG8_SCHED;
;             PG8_LDA(At, 1, 1); PG8_STAGE(PG8_SB(1, 0), b3, voffB); PG8_STAGE(PG8_SB(1, 1), b3 + hstep, voffB); PG8_STAGE(PG8_SA(1, 0), a3, ao[0]);
;             PG8_WAIT_V(8); PG8_WAIT_L(0); PG8_BAR; if (full) { PG8_MMA(1, 0, At, B0); PG8_MMA(1, 1, At, B1); } PG8_BAR; PG8_SCHED;
.LBB0_1449:
	s_add_i32 s89, s89, 2
	s_add_u32 s87, s87, 0x100
	s_addc_u32 s88, s88, 0
	s_add_u32 s60, s60, 0x100
	s_addc_u32 s61, s61, 0
	s_cmp_gt_u32 s89, 13
	s_barrier
	s_cbranch_scc1 .LBB0_1462

; #define PG8_STAGE(bufoff, gbase, voff) do { _Pragma("unroll") for (int _i = 0; _i < 2; ++_i) \
;         __builtin_amdgcn_global_load_lds((const unsigned*)((const char*)(gbase) + (voff)[_i]), (LAS unsigned*)(lds + (bufoff) + ldsw + _i * 8192), 16, 0, 0); } while (0)
; #define PG8_LDA(dst, b, h) do { _Pragma("unroll") for (int m = 0; m < 4; ++m) _Pragma("unroll") for (int k = 0; k < 2; ++k) frag_set(dst[m], k, *(const LAS bf16x8*)(lds + PG8_SA(b, h) + aoff + m * 2048 + k * 1024)); } while (0)
; template <class Epi, class Sched, bool ALIGN_EPI, bool FP8 = false>
; __device__ __forceinline__ void gemm_phase(LAS unsigned char* lds, const Gemm g, const Sched& S, const Epi& E) {
;     ...
;         for (int t = 0; t < nt; t += 2) {
;             const bool last = (t == nt - 2);
;             const char* a1 = Ab + (size_t)(t + 1) * kstep;
;             PG8_LDB(B0, 0, 0); PG8_LDB(B1, 0, 1); PG8_SCHED; PG8_LDA(At, 0, 0); PG8_STAGE(PG8_SA(1, 1), a1, ao[1]);
;             PG8_WAIT_V(8); PG8_WAIT_L(0); PG8_BAR; if (do0) { PG8_MMA(0, 0, At, B0); PG8_MMA(0, 1, At, B1); } PG8_BAR; PG8_SCHED;
;             const char* a2 = last ? Ab : Ab + (size_t)(t + 2) * kstep; const char* b2 = last ? nB : cB + (size_t)(t + 2) * kstep;
;             if (last && has_next) { int t2 = tid; asm volatile("" : "+v"(t2)); int R2[2], C2[2];
; #pragma unroll
;                 for (int i = 0; i < 2; ++i) stage_rc(t2 * 16 + i * 8192, R2[i], C2[i]);
;                 S.a_off_next(nxt, R2, C2, ao, lds + AUX_OFF); }
;             const char* a3 = a2 + kstep; const char* b3 = b2 + kstep;
;             PG8_LDA(At, 0, 1); PG8_STAGE(PG8_SB(0, 0), b2, voffB); PG8_STAGE(PG8_SB(0, 1), b2 + hstep, voffB); PG8_STAGE(PG8_SA(0, 0), a2, ao[0]);
;             PG8_WAIT_V(8); PG8_WAIT_L(0); PG8_BAR; if (full) { PG8_MMA(1, 0, At, B0); PG8_MMA(1, 1, At, B1); } PG8_BAR; PG8_SCHED;
;             PG8_LDB(B0, 1, 0); PG8_LDB(B1, 1, 1); PG8_SCHED; PG8_LDA(At, 1, 0); PG8_STAGE(PG8_SA(0, 1), a2, ao[1]);
;             PG8_WAIT_V(8); PG8_WAIT_L(0); PG8_BAR; if (do0) { PG8_MMA(0, 0, At, B0); PG8_MMA(0, 1, At, B1); } PG8_BAR; PG8_SCHED;
;             PG8_LDA(At, 1, 1); PG8_STAGE(PG8_SB(1, 0), b3, voffB); PG8_STAGE(PG8_SB(1, 1), b3 + hstep, voffB); PG8_STAGE(PG8_SA(1, 0), a3, ao[0]);
;             PG8_WAIT_V(8); PG8_WAIT_L(0); PG8_BAR; if (full) { PG8_MMA(1, 0, At, B0); PG8_MMA(1, 1, At, B1); } PG8_BAR; PG8_SCHED;
.LBB0_1512:
	s_add_i32 s6, s97, 2
	s_cmp_gt_u32 s97, 13
	s_barrier
	s_cbranch_scc1 .LBB0_1516
	s_mov_b32 s97, s6
	s_branch .LBB0_1498
